# attention steps: compiler pads after v_max3 asm blocks dropped, v_pk_add_f32 split into v_add_f32 pairs (bit-identical)
# speedup vs baseline: 1.0045x; 1.0045x over previous
.LBB0_1456:
	s_add_i32 s2, s79, 1
	s_and_b32 s2, s2, 3
	s_mulk_i32 s2, 0x3000
	v_add_u32_e32 v72, s2, v168
	ds_read_b128 v[68:71], v72
	ds_read_b128 v[172:175], v72 offset:512
	ds_read_b128 v[176:179], v72 offset:2048
	ds_read_b128 v[180:183], v72 offset:2560
	ds_read_b128 v[184:187], v72 offset:4096
	ds_read_b128 v[190:193], v72 offset:4608
	ds_read_b128 v[212:215], v72 offset:6144
	ds_read_b128 v[216:219], v72 offset:6656
	ds_read_b128 v[224:227], v72 offset:8192
	ds_read_b128 v[228:231], v72 offset:8704
	ds_read_b128 v[232:235], v72 offset:10240
	ds_read_b128 v[236:239], v72 offset:10752
	s_waitcnt lgkmcnt(11)
	v_mfma_f32_32x32x16_bf16 v[100:115], v[68:71], v[116:119], v[36:51]
	v_exp_f32_e32 v84, v84
	v_exp_f32_e32 v85, v85
	v_exp_f32_e32 v86, v86
	v_exp_f32_e32 v87, v87
	s_waitcnt lgkmcnt(10)
	v_mfma_f32_32x32x16_bf16 v[68:83], v[172:175], v[116:119], v[36:51]
	v_add_f32_e64 v172, v84, 0
	v_add_f32_e64 v173, v85, 0
	v_add_f32_e64 v172, v86, v172
	v_add_f32_e64 v173, v87, v173
	s_waitcnt lgkmcnt(9)
	v_mfma_f32_32x32x16_bf16 v[100:115], v[176:179], v[120:123], v[100:115]
	v_exp_f32_e32 v88, v88
	v_exp_f32_e32 v89, v89
	v_exp_f32_e32 v90, v90
	v_exp_f32_e32 v91, v91
	v_add_f32_e32 v172, v88, v172
	v_add_f32_e32 v173, v89, v173
	v_add_f32_e32 v172, v90, v172
	v_add_f32_e32 v173, v91, v173
	s_waitcnt lgkmcnt(8)
	v_mfma_f32_32x32x16_bf16 v[68:83], v[180:183], v[120:123], v[68:83]
	s_waitcnt lgkmcnt(7)
	v_mfma_f32_32x32x16_bf16 v[100:115], v[184:187], v[124:127], v[100:115]
	v_exp_f32_e32 v92, v92
	v_exp_f32_e32 v93, v93
	v_exp_f32_e32 v94, v94
	v_exp_f32_e32 v95, v95
	v_add_f32_e32 v172, v92, v172
	v_add_f32_e32 v173, v93, v173
	v_add_f32_e32 v172, v94, v172
	v_add_f32_e32 v173, v95, v173
	s_waitcnt lgkmcnt(6)
	v_mfma_f32_32x32x16_bf16 v[68:83], v[190:193], v[124:127], v[68:83]
	s_waitcnt lgkmcnt(5)
	v_mfma_f32_32x32x16_bf16 v[100:115], v[212:215], v[128:131], v[100:115]
	v_exp_f32_e32 v96, v96
	v_exp_f32_e32 v97, v97
	v_exp_f32_e32 v98, v98
	v_exp_f32_e32 v99, v99
	v_add_f32_e32 v172, v96, v172
	v_add_f32_e32 v173, v97, v173
	v_add_f32_e32 v172, v98, v172
	v_add_f32_e32 v173, v99, v173
	s_waitcnt lgkmcnt(4)
	v_mfma_f32_32x32x16_bf16 v[68:83], v[216:219], v[128:131], v[68:83]
	v_exp_f32_e32 v174, v52
	v_exp_f32_e32 v175, v53
	s_waitcnt lgkmcnt(3)
	v_mfma_f32_32x32x16_bf16 v[100:115], v[224:227], v[132:135], v[100:115]
	v_add_f32_e64 v52, v174, v172
	v_add_f32_e64 v53, v175, v173
	v_exp_f32_e32 v172, v54
	v_exp_f32_e32 v173, v55
	v_add_f32_e32 v52, v172, v52
	v_add_f32_e32 v53, v173, v53
	s_waitcnt lgkmcnt(2)
	v_mfma_f32_32x32x16_bf16 v[68:83], v[228:231], v[132:135], v[68:83]
	s_waitcnt lgkmcnt(1)
	v_mfma_f32_32x32x16_bf16 v[100:115], v[232:235], v[136:139], v[100:115]
	v_exp_f32_e32 v176, v56
	v_exp_f32_e32 v177, v57
	v_exp_f32_e32 v178, v58
	v_exp_f32_e32 v179, v59
	v_add_f32_e32 v52, v176, v52
	v_add_f32_e32 v53, v177, v53
	v_add_f32_e32 v194, v178, v52
	v_add_f32_e32 v195, v179, v53
	s_waitcnt lgkmcnt(0)
	v_mfma_f32_32x32x16_bf16 v[68:83], v[236:239], v[136:139], v[68:83]
	s_and_b32 s2, s78, 0x4000
	v_add_u32_e32 v212, s2, v2
	v_cvt_pk_bf16_f32 v54, v88, v89
	ds_read_b64_tr_b16 v[88:89],v212 offset:0
	v_cvt_pk_bf16_f32 v55, v90, v91
	ds_read_b64_tr_b16 v[90:91],v212 offset:512
	v_cvt_pk_bf16_f32 v53, v86, v87
	v_cvt_pk_bf16_f32 v86, v176, v177
	ds_read_b64_tr_b16 v[176:177],v212 offset:4096
	v_cvt_pk_bf16_f32 v87, v178, v179
	ds_read_b64_tr_b16 v[178:179],v212 offset:4608
	v_cvt_pk_bf16_f32 v56, v92, v93
	ds_read_b64_tr_b16 v[92:93],v212 offset:1024
	v_cvt_pk_bf16_f32 v57, v94, v95
	ds_read_b64_tr_b16 v[94:95],v212 offset:1536
	ds_read_b64_tr_b16 v[180:181],v212 offset:5120
	ds_read_b64_tr_b16 v[182:183],v212 offset:5632
	v_cvt_pk_bf16_f32 v58, v96, v97
	ds_read_b64_tr_b16 v[96:97],v212 offset:2048
	v_cvt_pk_bf16_f32 v59, v98, v99
	ds_read_b64_tr_b16 v[98:99],v212 offset:2560
	ds_read_b64_tr_b16 v[184:185],v212 offset:6144
	ds_read_b64_tr_b16 v[186:187],v212 offset:6656
	v_cvt_pk_bf16_f32 v52, v84, v85
	v_cvt_pk_bf16_f32 v85, v172, v173
	ds_read_b64_tr_b16 v[172:173],v212 offset:3072
	v_cvt_pk_bf16_f32 v84, v174, v175
	ds_read_b64_tr_b16 v[174:175],v212 offset:3584
	ds_read_b64_tr_b16 v[190:191],v212 offset:7168
	ds_read_b64_tr_b16 v[192:193],v212 offset:7680
	s_waitcnt lgkmcnt(14)
	v_mfma_f32_32x32x16_bf16 v[4:19], v[52:55], v[88:91], v[4:19]
	s_waitcnt lgkmcnt(12)
	v_mfma_f32_32x32x16_bf16 v[20:35], v[52:55], v[176:179], v[20:35]
	v_exp_f32_e32 v52, v60
	v_exp_f32_e32 v53, v61
	v_exp_f32_e32 v60, v62
	v_exp_f32_e32 v61, v63
	v_add_f32_e32 v54, v52, v194
	v_add_f32_e32 v55, v53, v195
	v_add_f32_e32 v54, v60, v54
	v_add_f32_e32 v55, v61, v55
	s_waitcnt lgkmcnt(10)
	v_mfma_f32_32x32x16_bf16 v[4:19], v[56:59], v[92:95], v[4:19]
	v_cvt_pk_bf16_f32 v52, v52, v53
	v_cvt_pk_bf16_f32 v53, v60, v61
	s_waitcnt lgkmcnt(8)
	v_mfma_f32_32x32x16_bf16 v[20:35], v[56:59], v[180:183], v[20:35]
	v_exp_f32_e32 v56, v64
	v_exp_f32_e32 v57, v65
	v_exp_f32_e32 v58, v66
	v_exp_f32_e32 v59, v67
	v_add_f32_e32 v54, v56, v54
	v_add_f32_e32 v55, v57, v55
	v_add_f32_e32 v62, v58, v54
	v_add_f32_e32 v63, v59, v55
	v_cvt_pk_bf16_f32 v54, v56, v57
	v_add_f32_e32 v56, v62, v63
	v_add_f32_e32 v171, v171, v56
	v_cvt_pk_bf16_f32 v55, v58, v59
	s_waitcnt lgkmcnt(6)
	v_mfma_f32_32x32x16_bf16 v[4:19], v[84:87], v[96:99], v[4:19]
	v_max3_f32 v56, v100, v68, v101
	v_max3_f32 v56, v56, v69, v102
	v_max3_f32 v56, v56, v70, v103
	v_max3_f32 v56, v56, v71, v104
	s_waitcnt lgkmcnt(4)
	v_mfma_f32_32x32x16_bf16 v[20:35], v[84:87], v[184:187], v[20:35]
	v_max3_f32 v56, v56, v72, v105
	v_max3_f32 v56, v56, v73, v106
	v_max3_f32 v56, v56, v74, v107
	v_max3_f32 v56, v56, v75, v107
	s_waitcnt lgkmcnt(2)
	v_mfma_f32_32x32x16_bf16 v[4:19], v[52:55], v[172:175], v[4:19]
	s_waitcnt lgkmcnt(0)
	v_mfma_f32_32x32x16_bf16 v[20:35], v[52:55], v[190:193], v[20:35]
	v_max3_f32 v52, v56, v108, v76
	v_max3_f32 v52, v52, v109, v77
	v_max3_f32 v52, v52, v110, v78
	v_max3_f32 v52, v52, v111, v79
	v_max3_f32 v52, v52, v112, v80
	v_max3_f32 v52, v52, v113, v81
	v_max3_f32 v52, v52, v114, v82
	v_max3_f32 v52, v52, v115, v83
	v_mov_b32_e32 v53, v52
	s_nop 1
	v_permlane32_swap_b32_e32 v52, v53
	v_max_f32_e32 v53, v53, v53
	v_max_f32_e32 v52, v52, v52
	v_max_f32_e32 v52, v52, v53
	v_cmp_lt_f32_e32 vcc, s13, v52
	s_cbranch_vccz .LBB0_1460
	v_max_f32_e32 v52, v52, v52
	v_max_f32_e32 v52, 0, v52
	v_exp_f32_e64 v53, -v52
	s_and_saveexec_b64 s[6:7], s[36:37]
	ds_write_b32 v170, v53
	s_or_b64 exec, exec, s[6:7]
	v_mul_f32_e32 v171, v171, v53
	s_waitcnt lgkmcnt(0)
	v_add_u32_e32 v53, s28, v169
	ds_read_b128 v[54:57], v53
	ds_read_b128 v[58:61], v53 offset:32
	ds_read_b128 v[62:65], v53 offset:64
	ds_read_b128 v[84:87], v53 offset:96
	s_waitcnt lgkmcnt(0)
	s_waitcnt lgkmcnt(3)
	v_pk_mul_f32 v[6:7], v[6:7], v[56:57]
	s_waitcnt lgkmcnt(2)
	v_pk_mul_f32 v[8:9], v[8:9], v[58:59]
	s_waitcnt lgkmcnt(1)
	v_pk_mul_f32 v[12:13], v[12:13], v[62:63]
	s_waitcnt lgkmcnt(0)
	v_pk_mul_f32 v[16:17], v[16:17], v[84:85]
	v_pk_mul_f32 v[18:19], v[18:19], v[86:87]
	v_pk_mul_f32 v[14:15], v[14:15], v[64:65]
	v_pk_mul_f32 v[10:11], v[10:11], v[60:61]
	v_pk_mul_f32 v[4:5], v[4:5], v[54:55]
	v_pk_mul_f32 v[32:33], v[32:33], v[84:85]
	v_pk_mul_f32 v[28:29], v[28:29], v[62:63]
	v_pk_mul_f32 v[24:25], v[24:25], v[58:59]
	v_pk_mul_f32 v[34:35], v[34:35], v[86:87]
	v_pk_mul_f32 v[30:31], v[30:31], v[64:65]
	v_pk_mul_f32 v[26:27], v[26:27], v[60:61]
	v_pk_mul_f32 v[22:23], v[22:23], v[56:57]
	v_pk_mul_f32 v[20:21], v[20:21], v[54:55]
	v_sub_f32_e32 v115, v115, v52
	v_sub_f32_e32 v114, v114, v52
	v_sub_f32_e32 v113, v113, v52
	v_sub_f32_e32 v112, v112, v52
	v_sub_f32_e32 v111, v111, v52
	v_sub_f32_e32 v110, v110, v52
	v_sub_f32_e32 v109, v109, v52
	v_sub_f32_e32 v108, v108, v52
	v_sub_f32_e32 v107, v107, v52
	v_sub_f32_e32 v106, v106, v52
	v_sub_f32_e32 v105, v105, v52
	v_sub_f32_e32 v104, v104, v52
	v_sub_f32_e32 v103, v103, v52
	v_sub_f32_e32 v102, v102, v52
	v_sub_f32_e32 v101, v101, v52
	v_sub_f32_e32 v100, v100, v52
	v_sub_f32_e32 v83, v83, v52
	v_sub_f32_e32 v82, v82, v52
	v_sub_f32_e32 v81, v81, v52
	v_sub_f32_e32 v80, v80, v52
	v_sub_f32_e32 v79, v79, v52
	v_sub_f32_e32 v78, v78, v52
	v_sub_f32_e32 v77, v77, v52
	v_sub_f32_e32 v76, v76, v52
	v_sub_f32_e32 v75, v75, v52
	v_sub_f32_e32 v74, v74, v52
	v_sub_f32_e32 v73, v73, v52
	v_sub_f32_e32 v72, v72, v52
	v_sub_f32_e32 v71, v71, v52
	v_sub_f32_e32 v70, v70, v52
	v_sub_f32_e32 v69, v69, v52
	v_sub_f32_e32 v68, v68, v52
	v_sub_f32_e32 v51, v51, v52
	v_sub_f32_e32 v50, v50, v52
	v_sub_f32_e32 v49, v49, v52
	v_sub_f32_e32 v48, v48, v52
	v_sub_f32_e32 v47, v47, v52
	v_sub_f32_e32 v46, v46, v52
	v_sub_f32_e32 v45, v45, v52
	v_sub_f32_e32 v44, v44, v52
	v_sub_f32_e32 v43, v43, v52
	v_sub_f32_e32 v42, v42, v52
	v_sub_f32_e32 v41, v41, v52
	v_sub_f32_e32 v40, v40, v52
	v_sub_f32_e32 v39, v39, v52
	v_sub_f32_e32 v38, v38, v52
	v_sub_f32_e32 v37, v37, v52
	v_sub_f32_e32 v36, v36, v52

.LBB0_1464:
	s_add_i32 s79, s79, 2
	s_and_b32 s2, s79, 2
	s_mulk_i32 s2, 0x3000
	v_add_u32_e32 v56, s2, v168
	ds_read_b128 v[52:55], v56
	ds_read_b128 v[172:175], v56 offset:512
	ds_read_b128 v[176:179], v56 offset:2048
	ds_read_b128 v[180:183], v56 offset:2560
	ds_read_b128 v[184:187], v56 offset:4096
	ds_read_b128 v[190:193], v56 offset:4608
	ds_read_b128 v[212:215], v56 offset:6144
	ds_read_b128 v[216:219], v56 offset:6656
	ds_read_b128 v[224:227], v56 offset:8192
	ds_read_b128 v[228:231], v56 offset:8704
	ds_read_b128 v[232:235], v56 offset:10240
	ds_read_b128 v[236:239], v56 offset:10752
	s_waitcnt lgkmcnt(11)
	v_mfma_f32_32x32x16_bf16 v[84:99], v[52:55], v[116:119], v[36:51]
	v_exp_f32_e32 v100, v100
	v_exp_f32_e32 v101, v101
	v_exp_f32_e32 v102, v102
	v_exp_f32_e32 v103, v103
	s_waitcnt lgkmcnt(10)
	v_mfma_f32_32x32x16_bf16 v[52:67], v[172:175], v[116:119], v[36:51]
	v_add_f32_e64 v172, v100, 0
	v_add_f32_e64 v173, v101, 0
	v_add_f32_e64 v172, v102, v172
	v_add_f32_e64 v173, v103, v173
	s_waitcnt lgkmcnt(9)
	v_mfma_f32_32x32x16_bf16 v[84:99], v[176:179], v[120:123], v[84:99]
	v_exp_f32_e32 v104, v104
	v_exp_f32_e32 v105, v105
	v_exp_f32_e32 v106, v106
	v_exp_f32_e32 v107, v107
	v_add_f32_e32 v172, v104, v172
	v_add_f32_e32 v173, v105, v173
	v_add_f32_e32 v172, v106, v172
	v_add_f32_e32 v173, v107, v173
	s_waitcnt lgkmcnt(8)
	v_mfma_f32_32x32x16_bf16 v[52:67], v[180:183], v[120:123], v[52:67]
	s_waitcnt lgkmcnt(7)
	v_mfma_f32_32x32x16_bf16 v[84:99], v[184:187], v[124:127], v[84:99]
	v_exp_f32_e32 v108, v108
	v_exp_f32_e32 v109, v109
	v_exp_f32_e32 v110, v110
	v_exp_f32_e32 v111, v111
	v_add_f32_e32 v172, v108, v172
	v_add_f32_e32 v173, v109, v173
	v_add_f32_e32 v172, v110, v172
	v_add_f32_e32 v173, v111, v173
	s_waitcnt lgkmcnt(6)
	v_mfma_f32_32x32x16_bf16 v[52:67], v[190:193], v[124:127], v[52:67]
	s_waitcnt lgkmcnt(5)
	v_mfma_f32_32x32x16_bf16 v[84:99], v[212:215], v[128:131], v[84:99]
	v_exp_f32_e32 v112, v112
	v_exp_f32_e32 v113, v113
	v_exp_f32_e32 v114, v114
	v_exp_f32_e32 v115, v115
	v_add_f32_e32 v172, v112, v172
	v_add_f32_e32 v173, v113, v173
	v_add_f32_e32 v172, v114, v172
	v_add_f32_e32 v173, v115, v173
	s_waitcnt lgkmcnt(4)
	v_mfma_f32_32x32x16_bf16 v[52:67], v[216:219], v[128:131], v[52:67]
	v_exp_f32_e32 v174, v68
	v_exp_f32_e32 v175, v69
	s_waitcnt lgkmcnt(3)
	v_mfma_f32_32x32x16_bf16 v[84:99], v[224:227], v[132:135], v[84:99]
	v_add_f32_e64 v68, v174, v172
	v_add_f32_e64 v69, v175, v173
	v_exp_f32_e32 v172, v70
	v_exp_f32_e32 v173, v71
	v_add_f32_e32 v68, v172, v68
	v_add_f32_e32 v69, v173, v69
	s_waitcnt lgkmcnt(2)
	v_mfma_f32_32x32x16_bf16 v[52:67], v[228:231], v[132:135], v[52:67]
	s_waitcnt lgkmcnt(1)
	v_mfma_f32_32x32x16_bf16 v[84:99], v[232:235], v[136:139], v[84:99]
	v_exp_f32_e32 v176, v72
	v_exp_f32_e32 v177, v73
	v_exp_f32_e32 v178, v74
	v_exp_f32_e32 v179, v75
	v_add_f32_e32 v68, v176, v68
	v_add_f32_e32 v69, v177, v69
	v_add_f32_e32 v194, v178, v68
	v_add_f32_e32 v195, v179, v69
	s_waitcnt lgkmcnt(0)
	v_mfma_f32_32x32x16_bf16 v[52:67], v[236:239], v[136:139], v[52:67]
	s_add_i32 s2, s78, 0x2000
	s_and_b32 s2, s2, 0x6000
	v_add_u32_e32 v212, s2, v2
	v_cvt_pk_bf16_f32 v70, v104, v105
	ds_read_b64_tr_b16 v[104:105],v212 offset:0
	v_cvt_pk_bf16_f32 v71, v106, v107
	ds_read_b64_tr_b16 v[106:107],v212 offset:512
	v_cvt_pk_bf16_f32 v69, v102, v103
	v_cvt_pk_bf16_f32 v102, v176, v177
	ds_read_b64_tr_b16 v[176:177],v212 offset:4096
	v_cvt_pk_bf16_f32 v103, v178, v179
	ds_read_b64_tr_b16 v[178:179],v212 offset:4608
	v_cvt_pk_bf16_f32 v72, v108, v109
	ds_read_b64_tr_b16 v[108:109],v212 offset:1024
	v_cvt_pk_bf16_f32 v73, v110, v111
	ds_read_b64_tr_b16 v[110:111],v212 offset:1536
	ds_read_b64_tr_b16 v[180:181],v212 offset:5120
	ds_read_b64_tr_b16 v[182:183],v212 offset:5632
	v_cvt_pk_bf16_f32 v74, v112, v113
	ds_read_b64_tr_b16 v[112:113],v212 offset:2048
	v_cvt_pk_bf16_f32 v75, v114, v115
	ds_read_b64_tr_b16 v[114:115],v212 offset:2560
	ds_read_b64_tr_b16 v[184:185],v212 offset:6144
	ds_read_b64_tr_b16 v[186:187],v212 offset:6656
	v_cvt_pk_bf16_f32 v68, v100, v101
	v_cvt_pk_bf16_f32 v101, v172, v173
	ds_read_b64_tr_b16 v[172:173],v212 offset:3072
	v_cvt_pk_bf16_f32 v100, v174, v175
	ds_read_b64_tr_b16 v[174:175],v212 offset:3584
	ds_read_b64_tr_b16 v[190:191],v212 offset:7168
	ds_read_b64_tr_b16 v[192:193],v212 offset:7680
	s_waitcnt lgkmcnt(14)
	v_mfma_f32_32x32x16_bf16 v[4:19], v[68:71], v[104:107], v[4:19]
	s_waitcnt lgkmcnt(12)
	v_mfma_f32_32x32x16_bf16 v[20:35], v[68:71], v[176:179], v[20:35]
	v_exp_f32_e32 v68, v76
	v_exp_f32_e32 v69, v77
	v_exp_f32_e32 v76, v78
	v_exp_f32_e32 v77, v79
	v_add_f32_e32 v70, v68, v194
	v_add_f32_e32 v71, v69, v195
	v_add_f32_e32 v70, v76, v70
	v_add_f32_e32 v71, v77, v71
	s_waitcnt lgkmcnt(10)
	v_mfma_f32_32x32x16_bf16 v[4:19], v[72:75], v[108:111], v[4:19]
	v_cvt_pk_bf16_f32 v68, v68, v69
	v_cvt_pk_bf16_f32 v69, v76, v77
	s_waitcnt lgkmcnt(8)
	v_mfma_f32_32x32x16_bf16 v[20:35], v[72:75], v[180:183], v[20:35]
	v_exp_f32_e32 v72, v80
	v_exp_f32_e32 v73, v81
	v_exp_f32_e32 v74, v82
	v_exp_f32_e32 v75, v83
	v_add_f32_e32 v70, v72, v70
	v_add_f32_e32 v71, v73, v71
	v_add_f32_e32 v78, v74, v70
	v_add_f32_e32 v79, v75, v71
	v_cvt_pk_bf16_f32 v70, v72, v73
	v_add_f32_e32 v72, v78, v79
	v_add_f32_e32 v171, v171, v72
	v_cvt_pk_bf16_f32 v71, v74, v75
	s_waitcnt lgkmcnt(6)
	v_mfma_f32_32x32x16_bf16 v[4:19], v[100:103], v[112:115], v[4:19]
	v_max3_f32 v72, v84, v52, v85
	v_max3_f32 v72, v72, v53, v86
	v_max3_f32 v72, v72, v54, v87
	v_max3_f32 v72, v72, v55, v88
	s_waitcnt lgkmcnt(4)
	v_mfma_f32_32x32x16_bf16 v[20:35], v[100:103], v[184:187], v[20:35]
	v_max3_f32 v72, v72, v56, v89
	v_max3_f32 v72, v72, v57, v90
	v_max3_f32 v72, v72, v58, v91
	v_max3_f32 v72, v72, v59, v91
	s_waitcnt lgkmcnt(2)
	v_mfma_f32_32x32x16_bf16 v[4:19], v[68:71], v[172:175], v[4:19]
	s_waitcnt lgkmcnt(0)
	v_mfma_f32_32x32x16_bf16 v[20:35], v[68:71], v[190:193], v[20:35]
	v_max3_f32 v68, v72, v92, v60
	v_max3_f32 v68, v68, v93, v61
	v_max3_f32 v68, v68, v94, v62
	v_max3_f32 v68, v68, v95, v63
	v_max3_f32 v68, v68, v96, v64
	v_max3_f32 v68, v68, v97, v65
	v_max3_f32 v68, v68, v98, v66
	v_max3_f32 v68, v68, v99, v67
	v_mov_b32_e32 v69, v68
	s_nop 1
	v_permlane32_swap_b32_e32 v68, v69
	s_andn2_b64 vcc, exec, s[62:63]
	s_cbranch_vccnz .LBB0_1451
	v_max_f32_e32 v68, v68, v68
	v_max_f32_e32 v69, v69, v69
	v_max_f32_e32 v68, v68, v69
	v_cmp_lt_f32_e32 vcc, s13, v68
	s_cbranch_vccz .LBB0_1451
	v_max_f32_e32 v68, v68, v68
	v_max_f32_e32 v68, 0, v68
	v_exp_f32_e64 v69, -v68
	s_and_saveexec_b64 s[6:7], s[36:37]
	s_cbranch_execz .LBB0_1450
	ds_write_b32 v170, v69
	s_branch .LBB0_1450

.LBB0_1576:
	v_pk_add_f32 v[116:117], v[68:69], 0 op_sel_hi:[1,0]
	v_exp_f32_e32 v76, v76
	v_exp_f32_e32 v77, v77
	v_add_f32_e32 v116, v70, v116
	v_add_f32_e32 v117, v71, v117
	v_exp_f32_e32 v78, v78
	v_exp_f32_e32 v79, v79
	v_add_f32_e32 v116, v72, v116
	v_add_f32_e32 v117, v73, v117
	v_exp_f32_e32 v80, v80
	v_exp_f32_e32 v81, v81
	v_add_f32_e32 v116, v74, v116
	v_add_f32_e32 v117, v75, v117
	v_exp_f32_e32 v82, v82
	v_exp_f32_e32 v83, v83
	v_add_f32_e32 v116, v76, v116
	v_add_f32_e32 v117, v77, v117
	v_exp_f32_e32 v52, v52
	v_exp_f32_e32 v53, v53
	v_add_f32_e32 v116, v78, v116
	v_add_f32_e32 v117, v79, v117
	v_exp_f32_e32 v54, v54
	v_exp_f32_e32 v55, v55
	v_add_f32_e32 v116, v80, v116
	v_add_f32_e32 v117, v81, v117
	v_exp_f32_e32 v56, v56
	v_exp_f32_e32 v57, v57
	v_add_f32_e32 v116, v82, v116
	v_add_f32_e32 v117, v83, v117
	v_exp_f32_e32 v58, v58
	v_exp_f32_e32 v59, v59
	v_add_f32_e32 v116, v52, v116
	v_add_f32_e32 v117, v53, v117
	v_exp_f32_e32 v60, v60
	v_exp_f32_e32 v61, v61
	v_add_f32_e32 v116, v54, v116
	v_add_f32_e32 v117, v55, v117
	v_exp_f32_e32 v62, v62
	v_exp_f32_e32 v63, v63
	v_add_f32_e32 v116, v56, v116
	v_add_f32_e32 v117, v57, v117
	v_cvt_pk_bf16_f32 v118, v80, v81
	v_add_f32_e32 v124, v58, v116
	v_add_f32_e32 v125, v59, v117
	v_cvt_pk_bf16_f32 v116, v76, v77
	v_cvt_pk_bf16_f32 v117, v78, v79
	v_add_f32_e32 v124, v60, v124
	v_add_f32_e32 v125, v61, v125
	v_cvt_pk_bf16_f32 v119, v82, v83
	v_cvt_pk_bf16_f32 v120, v52, v53
	v_cvt_pk_bf16_f32 v121, v54, v55
	v_cvt_pk_bf16_f32 v122, v56, v57
	v_cvt_pk_bf16_f32 v123, v58, v59
	v_add_f32_e32 v124, v62, v124
	v_add_f32_e32 v125, v63, v125
	s_waitcnt lgkmcnt(10)
	v_mfma_f32_32x32x16_bf16 v[4:19], v[116:119], v[180:183], v[4:19]
	v_exp_f32_e32 v64, v64
	v_exp_f32_e32 v65, v65
	v_exp_f32_e32 v66, v66
	v_exp_f32_e32 v67, v67
	s_waitcnt lgkmcnt(8)
	v_mfma_f32_32x32x16_bf16 v[20:35], v[116:119], v[184:187], v[20:35]
	v_add_f32_e64 v116, v64, v124
	v_add_f32_e64 v117, v65, v125
	v_cvt_pk_bf16_f32 v118, v64, v65
	v_add_f32_e64 v124, v66, v116
	v_add_f32_e64 v125, v67, v117
	v_cvt_pk_bf16_f32 v116, v60, v61
	v_add_f32_e32 v124, v124, v125
	v_cvt_pk_bf16_f32 v117, v62, v63
	v_add_f32_e32 v216, v216, v124
	v_cvt_pk_bf16_f32 v119, v66, v67
	s_waitcnt lgkmcnt(6)
	v_mfma_f32_32x32x16_bf16 v[4:19], v[120:123], v[176:179], v[4:19]
	v_max3_f32 v124, v100, v84, v101
	v_max3_f32 v124, v124, v85, v102
	v_max3_f32 v124, v124, v86, v103
	v_max3_f32 v124, v124, v87, v104
	s_waitcnt lgkmcnt(4)
	v_mfma_f32_32x32x16_bf16 v[20:35], v[120:123], v[172:175], v[20:35]
	v_max3_f32 v124, v124, v88, v105
	v_max3_f32 v124, v124, v89, v106
	v_max3_f32 v124, v124, v90, v107
	v_max3_f32 v124, v124, v91, v107
	s_waitcnt lgkmcnt(2)
	v_mfma_f32_32x32x16_bf16 v[4:19], v[116:119], v[164:167], v[4:19]
	s_waitcnt lgkmcnt(0)
	v_mfma_f32_32x32x16_bf16 v[20:35], v[116:119], v[168:171], v[20:35]
	v_max3_f32 v116, v124, v108, v92
	v_max3_f32 v116, v116, v109, v93
	v_max3_f32 v116, v116, v110, v94
	v_max3_f32 v116, v116, v111, v95
	v_max3_f32 v116, v116, v112, v96
	v_max3_f32 v116, v116, v113, v97
	v_max3_f32 v116, v116, v114, v98
	v_max3_f32 v116, v116, v115, v99
	v_mov_b32_e32 v117, v116
	s_nop 1
	v_permlane32_swap_b32_e32 v116, v117
	s_cmp_lt_i32 s6, s54
	s_cselect_b64 s[50:51], -1, 0
	s_cmp_ge_i32 s6, s54
	s_cbranch_scc1 .LBB0_1581
	v_max_f32_e32 v116, v116, v116
	v_max_f32_e32 v117, v117, v117
	v_max_f32_e32 v116, v116, v117
	v_cmp_lt_f32_e32 vcc, s13, v116
	s_cbranch_vccz .LBB0_1581
	v_max_f32_e32 v116, v116, v116
	v_max_f32_e32 v116, 0, v116
	v_exp_f32_e64 v117, -v116
	s_and_saveexec_b64 s[6:7], s[38:39]
	ds_write_b32 v2, v117
	s_or_b64 exec, exec, s[6:7]
	v_mul_f32_e32 v216, v216, v117
	s_waitcnt lgkmcnt(0)
	v_add_u32_e32 v117, s28, v190
	ds_read_b128 v[118:121], v117
	ds_read_b128 v[122:125], v117 offset:32
	ds_read_b128 v[126:129], v117 offset:64
	ds_read_b128 v[130:133], v117 offset:96
	s_waitcnt lgkmcnt(0)
	s_waitcnt lgkmcnt(3)
	v_pk_mul_f32 v[6:7], v[6:7], v[120:121]
	s_waitcnt lgkmcnt(2)
	v_pk_mul_f32 v[8:9], v[8:9], v[122:123]
	s_waitcnt lgkmcnt(1)
	v_pk_mul_f32 v[12:13], v[12:13], v[126:127]
	s_waitcnt lgkmcnt(0)
	v_pk_mul_f32 v[16:17], v[16:17], v[130:131]
	v_pk_mul_f32 v[18:19], v[18:19], v[132:133]
	v_pk_mul_f32 v[14:15], v[14:15], v[128:129]
	v_pk_mul_f32 v[10:11], v[10:11], v[124:125]
	v_pk_mul_f32 v[4:5], v[4:5], v[118:119]
	v_pk_mul_f32 v[32:33], v[32:33], v[130:131]
	v_pk_mul_f32 v[28:29], v[28:29], v[126:127]
	v_pk_mul_f32 v[24:25], v[24:25], v[122:123]
	v_pk_mul_f32 v[34:35], v[34:35], v[132:133]
	v_pk_mul_f32 v[30:31], v[30:31], v[128:129]
	v_pk_mul_f32 v[26:27], v[26:27], v[124:125]
	v_pk_mul_f32 v[22:23], v[22:23], v[120:121]
	v_pk_mul_f32 v[20:21], v[20:21], v[118:119]
	v_sub_f32_e32 v115, v115, v116
	v_sub_f32_e32 v114, v114, v116
	v_sub_f32_e32 v113, v113, v116
	v_sub_f32_e32 v112, v112, v116
	v_sub_f32_e32 v111, v111, v116
	v_sub_f32_e32 v110, v110, v116
	v_sub_f32_e32 v109, v109, v116
	v_sub_f32_e32 v108, v108, v116
	v_sub_f32_e32 v107, v107, v116
	v_sub_f32_e32 v106, v106, v116
	v_sub_f32_e32 v105, v105, v116
	v_sub_f32_e32 v104, v104, v116
	v_sub_f32_e32 v103, v103, v116
	v_sub_f32_e32 v102, v102, v116
	v_sub_f32_e32 v101, v101, v116
	v_sub_f32_e32 v100, v100, v116
	v_sub_f32_e32 v99, v99, v116
	v_sub_f32_e32 v98, v98, v116
	v_sub_f32_e32 v97, v97, v116
	v_sub_f32_e32 v96, v96, v116
	v_sub_f32_e32 v95, v95, v116
	v_sub_f32_e32 v94, v94, v116
	v_sub_f32_e32 v93, v93, v116
	v_sub_f32_e32 v92, v92, v116
	v_sub_f32_e32 v91, v91, v116
	v_sub_f32_e32 v90, v90, v116
	v_sub_f32_e32 v89, v89, v116
	v_sub_f32_e32 v88, v88, v116
	v_sub_f32_e32 v87, v87, v116
	v_sub_f32_e32 v86, v86, v116
	v_sub_f32_e32 v85, v85, v116
	v_sub_f32_e32 v84, v84, v116
	v_sub_f32_e32 v51, v51, v116
	v_sub_f32_e32 v50, v50, v116
	v_sub_f32_e32 v49, v49, v116
	v_sub_f32_e32 v48, v48, v116
	v_sub_f32_e32 v47, v47, v116
	v_sub_f32_e32 v46, v46, v116
	v_sub_f32_e32 v45, v45, v116
	v_sub_f32_e32 v44, v44, v116
	v_sub_f32_e32 v43, v43, v116
	v_sub_f32_e32 v42, v42, v116
	v_sub_f32_e32 v41, v41, v116
	v_sub_f32_e32 v40, v40, v116
	v_sub_f32_e32 v39, v39, v116
	v_sub_f32_e32 v38, v38, v116
	v_sub_f32_e32 v37, v37, v116
	v_sub_f32_e32 v36, v36, v116

.LBB0_1597:
	v_pk_add_f32 v[116:117], v[180:181], 0 op_sel_hi:[1,0]
	v_exp_f32_e32 v108, v108
	v_exp_f32_e32 v109, v109
	v_add_f32_e32 v116, v182, v116
	v_add_f32_e32 v117, v183, v117
	v_exp_f32_e32 v110, v110
	v_exp_f32_e32 v111, v111
	v_add_f32_e32 v116, v184, v116
	v_add_f32_e32 v117, v185, v117
	v_exp_f32_e32 v112, v112
	v_exp_f32_e32 v113, v113
	v_add_f32_e32 v116, v186, v116
	v_add_f32_e32 v117, v187, v117
	v_exp_f32_e32 v114, v114
	v_exp_f32_e32 v115, v115
	v_add_f32_e32 v116, v108, v116
	v_add_f32_e32 v117, v109, v117
	v_exp_f32_e32 v118, v84
	v_exp_f32_e32 v119, v85
	v_add_f32_e32 v116, v110, v116
	v_add_f32_e32 v117, v111, v117
	v_exp_f32_e32 v120, v86
	v_exp_f32_e32 v121, v87
	v_add_f32_e32 v116, v112, v116
	v_add_f32_e32 v117, v113, v117
	v_exp_f32_e32 v122, v88
	v_exp_f32_e32 v123, v89
	v_add_f32_e32 v116, v114, v116
	v_add_f32_e32 v117, v115, v117
	v_exp_f32_e32 v124, v90
	v_exp_f32_e32 v125, v91
	v_add_f32_e32 v84, v118, v116
	v_add_f32_e32 v85, v119, v117
	v_exp_f32_e32 v92, v92
	v_exp_f32_e32 v93, v93
	v_add_f32_e32 v84, v120, v84
	v_add_f32_e32 v85, v121, v85
	v_exp_f32_e32 v94, v94
	v_exp_f32_e32 v95, v95
	v_add_f32_e32 v84, v122, v84
	v_add_f32_e32 v85, v123, v85
	v_cvt_pk_bf16_f32 v86, v112, v113
	v_add_f32_e32 v116, v124, v84
	v_add_f32_e32 v117, v125, v85
	v_cvt_pk_bf16_f32 v84, v108, v109
	v_cvt_pk_bf16_f32 v85, v110, v111
	v_add_f32_e32 v108, v92, v116
	v_add_f32_e32 v109, v93, v117
	v_cvt_pk_bf16_f32 v87, v114, v115
	v_cvt_pk_bf16_f32 v88, v118, v119
	v_cvt_pk_bf16_f32 v89, v120, v121
	v_cvt_pk_bf16_f32 v90, v122, v123
	v_cvt_pk_bf16_f32 v91, v124, v125
	v_add_f32_e32 v108, v94, v108
	v_add_f32_e32 v109, v95, v109
	s_waitcnt lgkmcnt(10)
	v_mfma_f32_32x32x16_bf16 v[4:19], v[84:87], v[172:175], v[4:19]
	s_waitcnt lgkmcnt(8)
	v_mfma_f32_32x32x16_bf16 v[20:35], v[84:87], v[176:179], v[20:35]
	v_exp_f32_e32 v86, v96
	v_exp_f32_e32 v87, v97
	v_exp_f32_e32 v96, v98
	v_exp_f32_e32 v97, v99
	v_add_f32_e32 v84, v86, v108
	v_add_f32_e32 v85, v87, v109
	v_cvt_pk_bf16_f32 v86, v86, v87
	v_add_f32_e32 v98, v96, v84
	v_add_f32_e32 v99, v97, v85
	v_cvt_pk_bf16_f32 v84, v92, v93
	v_add_f32_e32 v92, v98, v99
	v_cvt_pk_bf16_f32 v85, v94, v95
	v_add_f32_e32 v216, v216, v92
	v_cvt_pk_bf16_f32 v87, v96, v97
	s_waitcnt lgkmcnt(6)
	v_mfma_f32_32x32x16_bf16 v[4:19], v[88:91], v[168:171], v[4:19]
	v_max3_f32 v92, v68, v52, v69
	v_max3_f32 v92, v92, v53, v70
	v_max3_f32 v92, v92, v54, v71
	v_max3_f32 v92, v92, v55, v72
	s_waitcnt lgkmcnt(4)
	v_mfma_f32_32x32x16_bf16 v[20:35], v[88:91], v[164:167], v[20:35]
	v_max3_f32 v92, v92, v56, v73
	v_max3_f32 v92, v92, v57, v74
	v_max3_f32 v92, v92, v58, v75
	v_max3_f32 v92, v92, v59, v75
	s_waitcnt lgkmcnt(2)
	v_mfma_f32_32x32x16_bf16 v[4:19], v[84:87], v[100:103], v[4:19]
	s_waitcnt lgkmcnt(0)
	v_mfma_f32_32x32x16_bf16 v[20:35], v[84:87], v[104:107], v[20:35]
	v_max3_f32 v84, v92, v76, v60
	v_max3_f32 v84, v84, v77, v61
	v_max3_f32 v84, v84, v78, v62
	v_max3_f32 v84, v84, v79, v63
	v_max3_f32 v84, v84, v80, v64
	v_max3_f32 v84, v84, v81, v65
	v_max3_f32 v84, v84, v82, v66
	v_max3_f32 v84, v84, v83, v67
	v_mov_b32_e32 v85, v84
	s_nop 1
	v_permlane32_swap_b32_e32 v84, v85
	s_andn2_b64 vcc, exec, s[48:49]
	s_cbranch_vccnz .LBB0_1602
	v_max_f32_e32 v84, v84, v84
	v_max_f32_e32 v85, v85, v85
	v_max_f32_e32 v84, v84, v85
	v_cmp_lt_f32_e32 vcc, s13, v84
	s_cbranch_vccz .LBB0_1602
	v_max_f32_e32 v84, v84, v84
	v_max_f32_e32 v84, 0, v84
	v_exp_f32_e64 v85, -v84
	s_and_saveexec_b64 s[6:7], s[38:39]
	ds_write_b32 v2, v85
	s_or_b64 exec, exec, s[6:7]
	v_mul_f32_e32 v216, v216, v85
	s_waitcnt lgkmcnt(0)
	v_add_u32_e32 v85, s28, v190
	ds_read_b128 v[86:89], v85
	ds_read_b128 v[90:93], v85 offset:32
	ds_read_b128 v[94:97], v85 offset:64
	ds_read_b128 v[98:101], v85 offset:96
	s_waitcnt lgkmcnt(0)
	s_waitcnt lgkmcnt(3)
	v_pk_mul_f32 v[6:7], v[6:7], v[88:89]
	s_waitcnt lgkmcnt(2)
	v_pk_mul_f32 v[8:9], v[8:9], v[90:91]
	s_waitcnt lgkmcnt(1)
	v_pk_mul_f32 v[12:13], v[12:13], v[94:95]
	s_waitcnt lgkmcnt(0)
	v_pk_mul_f32 v[16:17], v[16:17], v[98:99]
	v_pk_mul_f32 v[18:19], v[18:19], v[100:101]
	v_pk_mul_f32 v[14:15], v[14:15], v[96:97]
	v_pk_mul_f32 v[10:11], v[10:11], v[92:93]
	v_pk_mul_f32 v[4:5], v[4:5], v[86:87]
	v_pk_mul_f32 v[32:33], v[32:33], v[98:99]
	v_pk_mul_f32 v[28:29], v[28:29], v[94:95]
	v_pk_mul_f32 v[24:25], v[24:25], v[90:91]
	v_pk_mul_f32 v[34:35], v[34:35], v[100:101]
	v_pk_mul_f32 v[30:31], v[30:31], v[96:97]
	v_pk_mul_f32 v[26:27], v[26:27], v[92:93]
	v_pk_mul_f32 v[22:23], v[22:23], v[88:89]
	v_pk_mul_f32 v[20:21], v[20:21], v[86:87]
	v_sub_f32_e32 v83, v83, v84
	v_sub_f32_e32 v82, v82, v84
	v_sub_f32_e32 v81, v81, v84
	v_sub_f32_e32 v80, v80, v84
	v_sub_f32_e32 v79, v79, v84
	v_sub_f32_e32 v78, v78, v84
	v_sub_f32_e32 v77, v77, v84
	v_sub_f32_e32 v76, v76, v84
	v_sub_f32_e32 v75, v75, v84
	v_sub_f32_e32 v74, v74, v84
	v_sub_f32_e32 v73, v73, v84
	v_sub_f32_e32 v72, v72, v84
	v_sub_f32_e32 v71, v71, v84
	v_sub_f32_e32 v70, v70, v84
	v_sub_f32_e32 v69, v69, v84
	v_sub_f32_e32 v68, v68, v84
	v_sub_f32_e32 v67, v67, v84
	v_sub_f32_e32 v66, v66, v84
	v_sub_f32_e32 v65, v65, v84
	v_sub_f32_e32 v64, v64, v84
	v_sub_f32_e32 v63, v63, v84
	v_sub_f32_e32 v62, v62, v84
	v_sub_f32_e32 v61, v61, v84
	v_sub_f32_e32 v60, v60, v84
	v_sub_f32_e32 v59, v59, v84
	v_sub_f32_e32 v58, v58, v84
	v_sub_f32_e32 v57, v57, v84
	v_sub_f32_e32 v56, v56, v84
	v_sub_f32_e32 v55, v55, v84
	v_sub_f32_e32 v54, v54, v84
	v_sub_f32_e32 v53, v53, v84
	v_sub_f32_e32 v52, v52, v84
	v_sub_f32_e32 v51, v51, v84
	v_sub_f32_e32 v50, v50, v84
	v_sub_f32_e32 v49, v49, v84
	v_sub_f32_e32 v48, v48, v84
	v_sub_f32_e32 v47, v47, v84
	v_sub_f32_e32 v46, v46, v84
	v_sub_f32_e32 v45, v45, v84
	v_sub_f32_e32 v44, v44, v84
	v_sub_f32_e32 v43, v43, v84
	v_sub_f32_e32 v42, v42, v84
	v_sub_f32_e32 v41, v41, v84
	v_sub_f32_e32 v40, v40, v84
	v_sub_f32_e32 v39, v39, v84
	v_sub_f32_e32 v38, v38, v84
	v_sub_f32_e32 v37, v37, v84
	v_sub_f32_e32 v36, v36, v84

.LBB0_1635:
	s_mul_i32 s2, s26, 0x3000
	v_add_u32_e32 v72, s2, v140
	ds_read_b128 v[68:71], v72 offset:12288
	ds_read_b128 v[148:151], v72 offset:12800
	ds_read_b128 v[152:155], v72 offset:14336
	ds_read_b128 v[156:159], v72 offset:14848
	ds_read_b128 v[160:163], v72 offset:16384
	ds_read_b128 v[164:167], v72 offset:16896
	ds_read_b128 v[168:171], v72 offset:18432
	ds_read_b128 v[172:175], v72 offset:18944
	s_waitcnt lgkmcnt(7)
	v_mfma_f32_32x32x16_bf16 v[100:115], v[68:71], v[116:119], v[36:51]
	v_exp_f32_e32 v84, v84
	v_exp_f32_e32 v85, v85
	v_exp_f32_e32 v86, v86
	v_exp_f32_e32 v87, v87
	v_exp_f32_e32 v88, v88
	v_exp_f32_e32 v89, v89
	v_pk_add_f32 v[144:145], v[84:85], 0 op_sel_hi:[1,0]
	s_waitcnt lgkmcnt(6)
	v_mfma_f32_32x32x16_bf16 v[68:83], v[148:151], v[116:119], v[36:51]
	v_add_f32_e64 v144, v86, v144
	v_add_f32_e64 v145, v87, v145
	v_add_f32_e64 v144, v88, v144
	v_add_f32_e64 v145, v89, v145
	s_waitcnt lgkmcnt(5)
	v_mfma_f32_32x32x16_bf16 v[100:115], v[152:155], v[120:123], v[100:115]
	v_exp_f32_e32 v90, v90
	v_exp_f32_e32 v91, v91
	v_exp_f32_e32 v92, v92
	v_exp_f32_e32 v93, v93
	v_exp_f32_e32 v94, v94
	v_exp_f32_e32 v95, v95
	v_add_f32_e32 v144, v90, v144
	v_add_f32_e32 v145, v91, v145
	s_waitcnt lgkmcnt(4)
	v_mfma_f32_32x32x16_bf16 v[68:83], v[156:159], v[120:123], v[68:83]
	v_add_f32_e64 v144, v92, v144
	v_add_f32_e64 v145, v93, v145
	v_add_f32_e64 v144, v94, v144
	v_add_f32_e64 v145, v95, v145
	s_waitcnt lgkmcnt(3)
	v_mfma_f32_32x32x16_bf16 v[100:115], v[160:163], v[124:127], v[100:115]
	v_exp_f32_e32 v96, v96
	v_exp_f32_e32 v97, v97
	v_exp_f32_e32 v98, v98
	v_exp_f32_e32 v99, v99
	v_exp_f32_e32 v148, v52
	v_exp_f32_e32 v149, v53
	v_add_f32_e32 v144, v96, v144
	v_add_f32_e32 v145, v97, v145
	s_waitcnt lgkmcnt(2)
	v_mfma_f32_32x32x16_bf16 v[68:83], v[164:167], v[124:127], v[68:83]
	v_add_f32_e64 v144, v98, v144
	v_add_f32_e64 v145, v99, v145
	v_add_f32_e64 v52, v148, v144
	v_add_f32_e64 v53, v149, v145
	s_waitcnt lgkmcnt(1)
	v_mfma_f32_32x32x16_bf16 v[100:115], v[168:171], v[128:131], v[100:115]
	v_exp_f32_e32 v144, v54
	v_exp_f32_e32 v145, v55
	v_exp_f32_e32 v150, v56
	v_exp_f32_e32 v151, v57
	v_exp_f32_e32 v152, v58
	v_exp_f32_e32 v153, v59
	v_add_f32_e32 v52, v144, v52
	v_add_f32_e32 v53, v145, v53
	s_waitcnt lgkmcnt(0)
	v_mfma_f32_32x32x16_bf16 v[68:83], v[172:175], v[128:131], v[68:83]
	v_add_f32_e64 v52, v150, v52
	v_add_f32_e64 v53, v151, v53
	v_add_f32_e64 v168, v152, v52
	v_add_f32_e64 v169, v153, v53
	v_cvt_pk_bf16_f32 v52, v84, v85
	v_cvt_pk_bf16_f32 v54, v88, v89
	v_cvt_pk_bf16_f32 v85, v144, v145
	v_lshl_add_u32 v144, s26, 13, v2
	ds_read_b64_tr_b16 v[88:89],v144 offset:0
	v_cvt_pk_bf16_f32 v55, v90, v91
	ds_read_b64_tr_b16 v[90:91],v144 offset:512
	v_cvt_pk_bf16_f32 v53, v86, v87
	v_cvt_pk_bf16_f32 v87, v152, v153
	ds_read_b64_tr_b16 v[152:153],v144 offset:4096
	ds_read_b64_tr_b16 v[154:155],v144 offset:4608
	v_cvt_pk_bf16_f32 v56, v92, v93
	ds_read_b64_tr_b16 v[92:93],v144 offset:1024
	v_cvt_pk_bf16_f32 v57, v94, v95
	ds_read_b64_tr_b16 v[94:95],v144 offset:1536
	ds_read_b64_tr_b16 v[156:157],v144 offset:5120
	ds_read_b64_tr_b16 v[158:159],v144 offset:5632
	v_cvt_pk_bf16_f32 v58, v96, v97
	ds_read_b64_tr_b16 v[96:97],v144 offset:2048
	v_cvt_pk_bf16_f32 v59, v98, v99
	ds_read_b64_tr_b16 v[98:99],v144 offset:2560
	ds_read_b64_tr_b16 v[160:161],v144 offset:6144
	ds_read_b64_tr_b16 v[162:163],v144 offset:6656
	v_cvt_pk_bf16_f32 v84, v148, v149
	ds_read_b64_tr_b16 v[148:149],v144 offset:3072
	v_cvt_pk_bf16_f32 v86, v150, v151
	ds_read_b64_tr_b16 v[150:151],v144 offset:3584
	ds_read_b64_tr_b16 v[164:165],v144 offset:7168
	ds_read_b64_tr_b16 v[166:167],v144 offset:7680
	s_waitcnt lgkmcnt(14)
	v_mfma_f32_32x32x16_bf16 v[4:19], v[52:55], v[88:91], v[4:19]
	s_waitcnt lgkmcnt(12)
	v_mfma_f32_32x32x16_bf16 v[20:35], v[52:55], v[152:155], v[20:35]
	v_exp_f32_e32 v52, v60
	v_exp_f32_e32 v53, v61
	v_exp_f32_e32 v60, v62
	v_exp_f32_e32 v61, v63
	v_add_f32_e32 v54, v52, v168
	v_add_f32_e32 v55, v53, v169
	v_add_f32_e32 v54, v60, v54
	v_add_f32_e32 v55, v61, v55
	s_waitcnt lgkmcnt(10)
	v_mfma_f32_32x32x16_bf16 v[4:19], v[56:59], v[92:95], v[4:19]
	v_cvt_pk_bf16_f32 v52, v52, v53
	v_cvt_pk_bf16_f32 v53, v60, v61
	s_waitcnt lgkmcnt(8)
	v_mfma_f32_32x32x16_bf16 v[20:35], v[56:59], v[156:159], v[20:35]
	v_exp_f32_e32 v56, v64
	v_exp_f32_e32 v57, v65
	v_exp_f32_e32 v58, v66
	v_exp_f32_e32 v59, v67
	v_add_f32_e32 v54, v56, v54
	v_add_f32_e32 v55, v57, v55
	v_add_f32_e32 v62, v58, v54
	v_add_f32_e32 v63, v59, v55
	v_cvt_pk_bf16_f32 v54, v56, v57
	v_add_f32_e32 v56, v62, v63
	v_add_f32_e32 v143, v143, v56
	v_cvt_pk_bf16_f32 v55, v58, v59
	s_waitcnt lgkmcnt(6)
	v_mfma_f32_32x32x16_bf16 v[4:19], v[84:87], v[96:99], v[4:19]
	v_max3_f32 v56, v100, v68, v101
	v_max3_f32 v56, v56, v69, v102
	v_max3_f32 v56, v56, v70, v103
	v_max3_f32 v56, v56, v71, v104
	s_waitcnt lgkmcnt(4)
	v_mfma_f32_32x32x16_bf16 v[20:35], v[84:87], v[160:163], v[20:35]
	v_max3_f32 v56, v56, v72, v105
	v_max3_f32 v56, v56, v73, v106
	v_max3_f32 v56, v56, v74, v107
	v_max3_f32 v56, v56, v75, v107
	s_waitcnt lgkmcnt(2)
	v_mfma_f32_32x32x16_bf16 v[4:19], v[52:55], v[148:151], v[4:19]
	s_waitcnt lgkmcnt(0)
	v_mfma_f32_32x32x16_bf16 v[20:35], v[52:55], v[164:167], v[20:35]
	v_max3_f32 v52, v56, v108, v76
	v_max3_f32 v52, v52, v109, v77
	v_max3_f32 v52, v52, v110, v78
	v_max3_f32 v52, v52, v111, v79
	v_max3_f32 v52, v52, v112, v80
	v_max3_f32 v52, v52, v113, v81
	v_max3_f32 v52, v52, v114, v82
	v_max3_f32 v52, v52, v115, v83
	v_mov_b32_e32 v53, v52
	s_nop 1
	v_permlane32_swap_b32_e32 v52, v53
	v_max_f32_e32 v53, v53, v53
	v_max_f32_e32 v52, v52, v52
	v_max_f32_e32 v52, v52, v53
	v_cmp_lt_f32_e32 vcc, s13, v52
	s_cbranch_vccz .LBB0_1639
	v_max_f32_e32 v52, v52, v52
	v_max_f32_e32 v52, 0, v52
	v_exp_f32_e64 v53, -v52
	s_and_saveexec_b64 s[6:7], s[36:37]
	ds_write_b32 v142, v53
	s_or_b64 exec, exec, s[6:7]
	v_mul_f32_e32 v143, v143, v53
	s_waitcnt lgkmcnt(0)
	v_add_u32_e32 v53, s24, v141
	ds_read_b128 v[54:57], v53
	ds_read_b128 v[58:61], v53 offset:32
	ds_read_b128 v[62:65], v53 offset:64
	ds_read_b128 v[84:87], v53 offset:96
	s_waitcnt lgkmcnt(0)
	s_waitcnt lgkmcnt(3)
	v_pk_mul_f32 v[6:7], v[6:7], v[56:57]
	s_waitcnt lgkmcnt(2)
	v_pk_mul_f32 v[8:9], v[8:9], v[58:59]
	s_waitcnt lgkmcnt(1)
	v_pk_mul_f32 v[12:13], v[12:13], v[62:63]
	s_waitcnt lgkmcnt(0)
	v_pk_mul_f32 v[16:17], v[16:17], v[84:85]
	v_pk_mul_f32 v[18:19], v[18:19], v[86:87]
	v_pk_mul_f32 v[14:15], v[14:15], v[64:65]
	v_pk_mul_f32 v[10:11], v[10:11], v[60:61]
	v_pk_mul_f32 v[4:5], v[4:5], v[54:55]
	v_pk_mul_f32 v[32:33], v[32:33], v[84:85]
	v_pk_mul_f32 v[28:29], v[28:29], v[62:63]
	v_pk_mul_f32 v[24:25], v[24:25], v[58:59]
	v_pk_mul_f32 v[34:35], v[34:35], v[86:87]
	v_pk_mul_f32 v[30:31], v[30:31], v[64:65]
	v_pk_mul_f32 v[26:27], v[26:27], v[60:61]
	v_pk_mul_f32 v[22:23], v[22:23], v[56:57]
	v_pk_mul_f32 v[20:21], v[20:21], v[54:55]
	v_sub_f32_e32 v115, v115, v52
	v_sub_f32_e32 v114, v114, v52
	v_sub_f32_e32 v113, v113, v52
	v_sub_f32_e32 v112, v112, v52
	v_sub_f32_e32 v111, v111, v52
	v_sub_f32_e32 v110, v110, v52
	v_sub_f32_e32 v109, v109, v52
	v_sub_f32_e32 v108, v108, v52
	v_sub_f32_e32 v107, v107, v52
	v_sub_f32_e32 v106, v106, v52
	v_sub_f32_e32 v105, v105, v52
	v_sub_f32_e32 v104, v104, v52
	v_sub_f32_e32 v103, v103, v52
	v_sub_f32_e32 v102, v102, v52
	v_sub_f32_e32 v101, v101, v52
	v_sub_f32_e32 v100, v100, v52
	v_sub_f32_e32 v83, v83, v52
	v_sub_f32_e32 v82, v82, v52
	v_sub_f32_e32 v81, v81, v52
	v_sub_f32_e32 v80, v80, v52
	v_sub_f32_e32 v79, v79, v52
	v_sub_f32_e32 v78, v78, v52
	v_sub_f32_e32 v77, v77, v52
	v_sub_f32_e32 v76, v76, v52
	v_sub_f32_e32 v75, v75, v52
	v_sub_f32_e32 v74, v74, v52
	v_sub_f32_e32 v73, v73, v52
	v_sub_f32_e32 v72, v72, v52
	v_sub_f32_e32 v71, v71, v52
	v_sub_f32_e32 v70, v70, v52
	v_sub_f32_e32 v69, v69, v52
	v_sub_f32_e32 v68, v68, v52
	v_sub_f32_e32 v51, v51, v52
	v_sub_f32_e32 v50, v50, v52
	v_sub_f32_e32 v49, v49, v52
	v_sub_f32_e32 v48, v48, v52
	v_sub_f32_e32 v47, v47, v52
	v_sub_f32_e32 v46, v46, v52
	v_sub_f32_e32 v45, v45, v52
	v_sub_f32_e32 v44, v44, v52
	v_sub_f32_e32 v43, v43, v52
	v_sub_f32_e32 v42, v42, v52
	v_sub_f32_e32 v41, v41, v52
	v_sub_f32_e32 v40, v40, v52
	v_sub_f32_e32 v39, v39, v52
	v_sub_f32_e32 v38, v38, v52
	v_sub_f32_e32 v37, v37, v52
	v_sub_f32_e32 v36, v36, v52

.LBB0_1643:
	s_xor_b32 s2, s26, 2
	s_mulk_i32 s2, 0x3000
	v_add_u32_e32 v56, s2, v140
	ds_read_b128 v[52:55], v56
	ds_read_b128 v[148:151], v56 offset:512
	ds_read_b128 v[152:155], v56 offset:2048
	ds_read_b128 v[156:159], v56 offset:2560
	ds_read_b128 v[160:163], v56 offset:4096
	ds_read_b128 v[164:167], v56 offset:4608
	ds_read_b128 v[168:171], v56 offset:6144
	ds_read_b128 v[172:175], v56 offset:6656
	s_waitcnt lgkmcnt(7)
	v_mfma_f32_32x32x16_bf16 v[84:99], v[52:55], v[116:119], v[36:51]
	v_exp_f32_e32 v100, v100
	v_exp_f32_e32 v101, v101
	v_exp_f32_e32 v102, v102
	v_exp_f32_e32 v103, v103
	v_exp_f32_e32 v104, v104
	v_exp_f32_e32 v105, v105
	s_waitcnt lgkmcnt(6)
	v_mfma_f32_32x32x16_bf16 v[52:67], v[148:151], v[116:119], v[36:51]
	v_add_f32_e64 v148, v100, 0
	v_add_f32_e64 v149, v101, 0
	v_add_f32_e64 v148, v102, v148
	v_add_f32_e64 v149, v103, v149
	v_add_f32_e64 v148, v104, v148
	v_add_f32_e64 v149, v105, v149
	s_waitcnt lgkmcnt(5)
	v_mfma_f32_32x32x16_bf16 v[84:99], v[152:155], v[120:123], v[84:99]
	v_exp_f32_e32 v106, v106
	v_exp_f32_e32 v107, v107
	v_exp_f32_e32 v108, v108
	v_exp_f32_e32 v109, v109
	v_exp_f32_e32 v110, v110
	v_exp_f32_e32 v111, v111
	v_add_f32_e32 v148, v106, v148
	v_add_f32_e32 v149, v107, v149
	s_waitcnt lgkmcnt(4)
	v_mfma_f32_32x32x16_bf16 v[52:67], v[156:159], v[120:123], v[52:67]
	v_add_f32_e64 v148, v108, v148
	v_add_f32_e64 v149, v109, v149
	v_add_f32_e64 v148, v110, v148
	v_add_f32_e64 v149, v111, v149
	s_waitcnt lgkmcnt(3)
	v_mfma_f32_32x32x16_bf16 v[84:99], v[160:163], v[124:127], v[84:99]
	v_exp_f32_e32 v112, v112
	v_exp_f32_e32 v113, v113
	v_exp_f32_e32 v114, v114
	v_exp_f32_e32 v115, v115
	v_exp_f32_e32 v150, v68
	v_exp_f32_e32 v151, v69
	v_add_f32_e32 v148, v112, v148
	v_add_f32_e32 v149, v113, v149
	s_waitcnt lgkmcnt(2)
	v_mfma_f32_32x32x16_bf16 v[52:67], v[164:167], v[124:127], v[52:67]
	v_add_f32_e64 v148, v114, v148
	v_add_f32_e64 v149, v115, v149
	v_add_f32_e64 v68, v150, v148
	v_add_f32_e64 v69, v151, v149
	s_waitcnt lgkmcnt(1)
	v_mfma_f32_32x32x16_bf16 v[84:99], v[168:171], v[128:131], v[84:99]
	v_exp_f32_e32 v148, v70
	v_exp_f32_e32 v149, v71
	v_exp_f32_e32 v152, v72
	v_exp_f32_e32 v153, v73
	v_exp_f32_e32 v154, v74
	v_exp_f32_e32 v155, v75
	v_add_f32_e32 v68, v148, v68
	v_add_f32_e32 v69, v149, v69
	s_waitcnt lgkmcnt(0)
	v_mfma_f32_32x32x16_bf16 v[52:67], v[172:175], v[128:131], v[52:67]
	v_add_f32_e64 v68, v152, v68
	v_add_f32_e64 v69, v153, v69
	v_add_f32_e64 v168, v154, v68
	v_add_f32_e64 v169, v155, v69
	v_add_u32_e32 v144, 0x2000, v144
	v_cvt_pk_bf16_f32 v70, v104, v105
	ds_read_b64_tr_b16 v[104:105],v144 offset:0
	v_cvt_pk_bf16_f32 v71, v106, v107
	ds_read_b64_tr_b16 v[106:107],v144 offset:512
	v_cvt_pk_bf16_f32 v69, v102, v103
	v_cvt_pk_bf16_f32 v102, v152, v153
	ds_read_b64_tr_b16 v[152:153],v144 offset:4096
	v_cvt_pk_bf16_f32 v103, v154, v155
	ds_read_b64_tr_b16 v[154:155],v144 offset:4608
	v_cvt_pk_bf16_f32 v72, v108, v109
	ds_read_b64_tr_b16 v[108:109],v144 offset:1024
	v_cvt_pk_bf16_f32 v73, v110, v111
	ds_read_b64_tr_b16 v[110:111],v144 offset:1536
	ds_read_b64_tr_b16 v[156:157],v144 offset:5120
	ds_read_b64_tr_b16 v[158:159],v144 offset:5632
	v_cvt_pk_bf16_f32 v74, v112, v113
	ds_read_b64_tr_b16 v[112:113],v144 offset:2048
	v_cvt_pk_bf16_f32 v75, v114, v115
	ds_read_b64_tr_b16 v[114:115],v144 offset:2560
	ds_read_b64_tr_b16 v[160:161],v144 offset:6144
	ds_read_b64_tr_b16 v[162:163],v144 offset:6656
	v_cvt_pk_bf16_f32 v68, v100, v101
	v_cvt_pk_bf16_f32 v101, v148, v149
	ds_read_b64_tr_b16 v[148:149],v144 offset:3072
	v_cvt_pk_bf16_f32 v100, v150, v151
	ds_read_b64_tr_b16 v[150:151],v144 offset:3584
	ds_read_b64_tr_b16 v[164:165],v144 offset:7168
	ds_read_b64_tr_b16 v[166:167],v144 offset:7680
	s_waitcnt lgkmcnt(14)
	v_mfma_f32_32x32x16_bf16 v[4:19], v[68:71], v[104:107], v[4:19]
	s_waitcnt lgkmcnt(12)
	v_mfma_f32_32x32x16_bf16 v[20:35], v[68:71], v[152:155], v[20:35]
	v_exp_f32_e32 v68, v76
	v_exp_f32_e32 v69, v77
	v_exp_f32_e32 v76, v78
	v_exp_f32_e32 v77, v79
	v_add_f32_e32 v70, v68, v168
	v_add_f32_e32 v71, v69, v169
	v_add_f32_e32 v70, v76, v70
	v_add_f32_e32 v71, v77, v71
	s_waitcnt lgkmcnt(10)
	v_mfma_f32_32x32x16_bf16 v[4:19], v[72:75], v[108:111], v[4:19]
	v_cvt_pk_bf16_f32 v68, v68, v69
	v_cvt_pk_bf16_f32 v69, v76, v77
	s_waitcnt lgkmcnt(8)
	v_mfma_f32_32x32x16_bf16 v[20:35], v[72:75], v[156:159], v[20:35]
	v_exp_f32_e32 v72, v80
	v_exp_f32_e32 v73, v81
	v_exp_f32_e32 v74, v82
	v_exp_f32_e32 v75, v83
	v_add_f32_e32 v70, v72, v70
	v_add_f32_e32 v71, v73, v71
	v_add_f32_e32 v78, v74, v70
	v_add_f32_e32 v79, v75, v71
	v_cvt_pk_bf16_f32 v70, v72, v73
	v_add_f32_e32 v72, v78, v79
	v_add_f32_e32 v143, v143, v72
	v_cvt_pk_bf16_f32 v71, v74, v75
	s_waitcnt lgkmcnt(6)
	v_mfma_f32_32x32x16_bf16 v[4:19], v[100:103], v[112:115], v[4:19]
	v_max3_f32 v72, v84, v52, v85
	v_max3_f32 v72, v72, v53, v86
	v_max3_f32 v72, v72, v54, v87
	v_max3_f32 v72, v72, v55, v88
	s_waitcnt lgkmcnt(4)
	v_mfma_f32_32x32x16_bf16 v[20:35], v[100:103], v[160:163], v[20:35]
	v_max3_f32 v72, v72, v56, v89
	v_max3_f32 v72, v72, v57, v90
	v_max3_f32 v72, v72, v58, v91
	v_max3_f32 v72, v72, v59, v91
	s_waitcnt lgkmcnt(2)
	v_mfma_f32_32x32x16_bf16 v[4:19], v[68:71], v[148:151], v[4:19]
	s_waitcnt lgkmcnt(0)
	v_mfma_f32_32x32x16_bf16 v[20:35], v[68:71], v[164:167], v[20:35]
	v_max3_f32 v68, v72, v92, v60
	v_max3_f32 v68, v68, v93, v61
	v_max3_f32 v68, v68, v94, v62
	v_max3_f32 v68, v68, v95, v63
	v_max3_f32 v68, v68, v96, v64
	v_max3_f32 v68, v68, v97, v65
	v_max3_f32 v68, v68, v98, v66
	v_max3_f32 v68, v68, v99, v67
	v_mov_b32_e32 v69, v68
	s_nop 1
	v_permlane32_swap_b32_e32 v68, v69
	s_and_b64 vcc, exec, s[38:39]
	s_cbranch_vccnz .LBB0_1630
	v_max_f32_e32 v68, v68, v68
	v_max_f32_e32 v69, v69, v69
	v_max_f32_e32 v68, v68, v69
	v_cmp_lt_f32_e32 vcc, s13, v68
	s_cbranch_vccz .LBB0_1630
	v_max_f32_e32 v68, v68, v68
	v_max_f32_e32 v68, 0, v68
	v_exp_f32_e64 v69, -v68
	s_and_saveexec_b64 s[6:7], s[36:37]
	s_cbranch_execz .LBB0_1629
	ds_write_b32 v142, v69
	s_branch .LBB0_1629

.LBB0_1667:
	s_or_b32 s25, s26, 1
	s_mul_i32 s2, s25, 0x3000
	v_add_u32_e32 v72, s2, v151
	ds_read_b128 v[68:71], v72
	ds_read_b128 v[156:159], v72 offset:512
	ds_read_b128 v[160:163], v72 offset:2048
	ds_read_b128 v[164:167], v72 offset:2560
	ds_read_b128 v[168:171], v72 offset:4096
	ds_read_b128 v[172:175], v72 offset:4608
	ds_read_b128 v[176:179], v72 offset:6144
	ds_read_b128 v[180:183], v72 offset:6656
	ds_read_b128 v[184:187], v72 offset:8192
	ds_read_b128 v[190:193], v72 offset:8704
	ds_read_b128 v[212:215], v72 offset:10240
	ds_read_b128 v[216:219], v72 offset:10752
	s_waitcnt lgkmcnt(11)
	v_mfma_f32_32x32x16_bf16 v[100:115], v[68:71], v[116:119], v[36:51]
	v_exp_f32_e32 v84, v84
	v_exp_f32_e32 v85, v85
	v_exp_f32_e32 v86, v86
	v_exp_f32_e32 v87, v87
	s_waitcnt lgkmcnt(10)
	v_mfma_f32_32x32x16_bf16 v[68:83], v[156:159], v[116:119], v[36:51]
	v_add_f32_e64 v156, v84, 0
	v_add_f32_e64 v157, v85, 0
	v_add_f32_e64 v156, v86, v156
	v_add_f32_e64 v157, v87, v157
	s_waitcnt lgkmcnt(9)
	v_mfma_f32_32x32x16_bf16 v[100:115], v[160:163], v[120:123], v[100:115]
	v_exp_f32_e32 v88, v88
	v_exp_f32_e32 v89, v89
	v_exp_f32_e32 v90, v90
	v_exp_f32_e32 v91, v91
	v_add_f32_e32 v156, v88, v156
	v_add_f32_e32 v157, v89, v157
	v_add_f32_e32 v156, v90, v156
	v_add_f32_e32 v157, v91, v157
	s_waitcnt lgkmcnt(8)
	v_mfma_f32_32x32x16_bf16 v[68:83], v[164:167], v[120:123], v[68:83]
	s_waitcnt lgkmcnt(7)
	v_mfma_f32_32x32x16_bf16 v[100:115], v[168:171], v[124:127], v[100:115]
	v_exp_f32_e32 v92, v92
	v_exp_f32_e32 v93, v93
	v_exp_f32_e32 v94, v94
	v_exp_f32_e32 v95, v95
	v_add_f32_e32 v156, v92, v156
	v_add_f32_e32 v157, v93, v157
	v_add_f32_e32 v156, v94, v156
	v_add_f32_e32 v157, v95, v157
	s_waitcnt lgkmcnt(6)
	v_mfma_f32_32x32x16_bf16 v[68:83], v[172:175], v[124:127], v[68:83]
	s_waitcnt lgkmcnt(5)
	v_mfma_f32_32x32x16_bf16 v[100:115], v[176:179], v[128:131], v[100:115]
	v_exp_f32_e32 v96, v96
	v_exp_f32_e32 v97, v97
	v_exp_f32_e32 v98, v98
	v_exp_f32_e32 v99, v99
	v_add_f32_e32 v156, v96, v156
	v_add_f32_e32 v157, v97, v157
	v_add_f32_e32 v156, v98, v156
	v_add_f32_e32 v157, v99, v157
	s_waitcnt lgkmcnt(4)
	v_mfma_f32_32x32x16_bf16 v[68:83], v[180:183], v[128:131], v[68:83]
	v_exp_f32_e32 v158, v52
	v_exp_f32_e32 v159, v53
	s_waitcnt lgkmcnt(3)
	v_mfma_f32_32x32x16_bf16 v[100:115], v[184:187], v[132:135], v[100:115]
	v_add_f32_e64 v52, v158, v156
	v_add_f32_e64 v53, v159, v157
	v_exp_f32_e32 v156, v54
	v_exp_f32_e32 v157, v55
	v_add_f32_e32 v52, v156, v52
	v_add_f32_e32 v53, v157, v53
	s_waitcnt lgkmcnt(2)
	v_mfma_f32_32x32x16_bf16 v[68:83], v[190:193], v[132:135], v[68:83]
	s_waitcnt lgkmcnt(1)
	v_mfma_f32_32x32x16_bf16 v[100:115], v[212:215], v[136:139], v[100:115]
	v_exp_f32_e32 v160, v56
	v_exp_f32_e32 v161, v57
	v_exp_f32_e32 v162, v58
	v_exp_f32_e32 v163, v59
	v_add_f32_e32 v52, v160, v52
	v_add_f32_e32 v53, v161, v53
	v_add_f32_e32 v176, v162, v52
	v_add_f32_e32 v177, v163, v53
	s_waitcnt lgkmcnt(0)
	v_mfma_f32_32x32x16_bf16 v[68:83], v[216:219], v[136:139], v[68:83]
	v_cvt_pk_bf16_f32 v54, v88, v89
	v_lshl_add_u32 v155, s26, 13, v2
	ds_read_b64_tr_b16 v[88:89],v155 offset:0
	v_cvt_pk_bf16_f32 v55, v90, v91
	ds_read_b64_tr_b16 v[90:91],v155 offset:512
	v_cvt_pk_bf16_f32 v53, v86, v87
	v_cvt_pk_bf16_f32 v86, v160, v161
	ds_read_b64_tr_b16 v[160:161],v155 offset:4096
	v_cvt_pk_bf16_f32 v87, v162, v163
	ds_read_b64_tr_b16 v[162:163],v155 offset:4608
	v_cvt_pk_bf16_f32 v56, v92, v93
	ds_read_b64_tr_b16 v[92:93],v155 offset:1024
	v_cvt_pk_bf16_f32 v57, v94, v95
	ds_read_b64_tr_b16 v[94:95],v155 offset:1536
	ds_read_b64_tr_b16 v[164:165],v155 offset:5120
	ds_read_b64_tr_b16 v[166:167],v155 offset:5632
	v_cvt_pk_bf16_f32 v58, v96, v97
	ds_read_b64_tr_b16 v[96:97],v155 offset:2048
	v_cvt_pk_bf16_f32 v59, v98, v99
	ds_read_b64_tr_b16 v[98:99],v155 offset:2560
	ds_read_b64_tr_b16 v[168:169],v155 offset:6144
	ds_read_b64_tr_b16 v[170:171],v155 offset:6656
	v_cvt_pk_bf16_f32 v52, v84, v85
	v_cvt_pk_bf16_f32 v85, v156, v157
	ds_read_b64_tr_b16 v[156:157],v155 offset:3072
	v_cvt_pk_bf16_f32 v84, v158, v159
	ds_read_b64_tr_b16 v[158:159],v155 offset:3584
	ds_read_b64_tr_b16 v[172:173],v155 offset:7168
	ds_read_b64_tr_b16 v[174:175],v155 offset:7680
	s_waitcnt lgkmcnt(14)
	v_mfma_f32_32x32x16_bf16 v[4:19], v[52:55], v[88:91], v[4:19]
	s_waitcnt lgkmcnt(12)
	v_mfma_f32_32x32x16_bf16 v[20:35], v[52:55], v[160:163], v[20:35]
	v_exp_f32_e32 v52, v60
	v_exp_f32_e32 v53, v61
	v_exp_f32_e32 v60, v62
	v_exp_f32_e32 v61, v63
	v_add_f32_e32 v54, v52, v176
	v_add_f32_e32 v55, v53, v177
	v_add_f32_e32 v54, v60, v54
	v_add_f32_e32 v55, v61, v55
	s_waitcnt lgkmcnt(10)
	v_mfma_f32_32x32x16_bf16 v[4:19], v[56:59], v[92:95], v[4:19]
	v_cvt_pk_bf16_f32 v52, v52, v53
	v_cvt_pk_bf16_f32 v53, v60, v61
	s_waitcnt lgkmcnt(8)
	v_mfma_f32_32x32x16_bf16 v[20:35], v[56:59], v[164:167], v[20:35]
	v_exp_f32_e32 v56, v64
	v_exp_f32_e32 v57, v65
	v_exp_f32_e32 v58, v66
	v_exp_f32_e32 v59, v67
	v_add_f32_e32 v54, v56, v54
	v_add_f32_e32 v55, v57, v55
	v_add_f32_e32 v62, v58, v54
	v_add_f32_e32 v63, v59, v55
	v_cvt_pk_bf16_f32 v54, v56, v57
	v_add_f32_e32 v56, v62, v63
	v_add_f32_e32 v154, v154, v56
	v_cvt_pk_bf16_f32 v55, v58, v59
	s_waitcnt lgkmcnt(6)
	v_mfma_f32_32x32x16_bf16 v[4:19], v[84:87], v[96:99], v[4:19]
	v_max3_f32 v56, v100, v68, v101
	v_max3_f32 v56, v56, v69, v102
	v_max3_f32 v56, v56, v70, v103
	v_max3_f32 v56, v56, v71, v104
	s_waitcnt lgkmcnt(4)
	v_mfma_f32_32x32x16_bf16 v[20:35], v[84:87], v[168:171], v[20:35]
	v_max3_f32 v56, v56, v72, v105
	v_max3_f32 v56, v56, v73, v106
	v_max3_f32 v56, v56, v74, v107
	v_max3_f32 v56, v56, v75, v107
	s_waitcnt lgkmcnt(2)
	v_mfma_f32_32x32x16_bf16 v[4:19], v[52:55], v[156:159], v[4:19]
	s_waitcnt lgkmcnt(0)
	v_mfma_f32_32x32x16_bf16 v[20:35], v[52:55], v[172:175], v[20:35]
	v_max3_f32 v52, v56, v108, v76
	v_max3_f32 v52, v52, v109, v77
	v_max3_f32 v52, v52, v110, v78
	v_max3_f32 v52, v52, v111, v79
	v_max3_f32 v52, v52, v112, v80
	v_max3_f32 v52, v52, v113, v81
	v_max3_f32 v52, v52, v114, v82
	v_max3_f32 v52, v52, v115, v83
	v_mov_b32_e32 v53, v52
	s_nop 1
	v_permlane32_swap_b32_e32 v52, v53
	v_max_f32_e32 v53, v53, v53
	v_max_f32_e32 v52, v52, v52
	v_max_f32_e32 v52, v52, v53
	v_cmp_lt_f32_e32 vcc, s13, v52
	s_cbranch_vccz .LBB0_1671
	v_max_f32_e32 v52, v52, v52
	v_max_f32_e32 v52, 0, v52
	v_exp_f32_e64 v53, -v52
	s_and_saveexec_b64 s[6:7], s[36:37]
	ds_write_b32 v153, v53
	s_or_b64 exec, exec, s[6:7]
	v_mul_f32_e32 v154, v154, v53
	s_waitcnt lgkmcnt(0)
	v_add_u32_e32 v53, s24, v152
	ds_read_b128 v[54:57], v53
	ds_read_b128 v[58:61], v53 offset:32
	ds_read_b128 v[62:65], v53 offset:64
	ds_read_b128 v[84:87], v53 offset:96
	s_waitcnt lgkmcnt(0)
	s_waitcnt lgkmcnt(3)
	v_pk_mul_f32 v[6:7], v[6:7], v[56:57]
	s_waitcnt lgkmcnt(2)
	v_pk_mul_f32 v[8:9], v[8:9], v[58:59]
	s_waitcnt lgkmcnt(1)
	v_pk_mul_f32 v[12:13], v[12:13], v[62:63]
	s_waitcnt lgkmcnt(0)
	v_pk_mul_f32 v[16:17], v[16:17], v[84:85]
	v_pk_mul_f32 v[18:19], v[18:19], v[86:87]
	v_pk_mul_f32 v[14:15], v[14:15], v[64:65]
	v_pk_mul_f32 v[10:11], v[10:11], v[60:61]
	v_pk_mul_f32 v[4:5], v[4:5], v[54:55]
	v_pk_mul_f32 v[32:33], v[32:33], v[84:85]
	v_pk_mul_f32 v[28:29], v[28:29], v[62:63]
	v_pk_mul_f32 v[24:25], v[24:25], v[58:59]
	v_pk_mul_f32 v[34:35], v[34:35], v[86:87]
	v_pk_mul_f32 v[30:31], v[30:31], v[64:65]
	v_pk_mul_f32 v[26:27], v[26:27], v[60:61]
	v_pk_mul_f32 v[22:23], v[22:23], v[56:57]
	v_pk_mul_f32 v[20:21], v[20:21], v[54:55]
	v_sub_f32_e32 v115, v115, v52
	v_sub_f32_e32 v114, v114, v52
	v_sub_f32_e32 v113, v113, v52
	v_sub_f32_e32 v112, v112, v52
	v_sub_f32_e32 v111, v111, v52
	v_sub_f32_e32 v110, v110, v52
	v_sub_f32_e32 v109, v109, v52
	v_sub_f32_e32 v108, v108, v52
	v_sub_f32_e32 v107, v107, v52
	v_sub_f32_e32 v106, v106, v52
	v_sub_f32_e32 v105, v105, v52
	v_sub_f32_e32 v104, v104, v52
	v_sub_f32_e32 v103, v103, v52
	v_sub_f32_e32 v102, v102, v52
	v_sub_f32_e32 v101, v101, v52
	v_sub_f32_e32 v100, v100, v52
	v_sub_f32_e32 v83, v83, v52
	v_sub_f32_e32 v82, v82, v52
	v_sub_f32_e32 v81, v81, v52
	v_sub_f32_e32 v80, v80, v52
	v_sub_f32_e32 v79, v79, v52
	v_sub_f32_e32 v78, v78, v52
	v_sub_f32_e32 v77, v77, v52
	v_sub_f32_e32 v76, v76, v52
	v_sub_f32_e32 v75, v75, v52
	v_sub_f32_e32 v74, v74, v52
	v_sub_f32_e32 v73, v73, v52
	v_sub_f32_e32 v72, v72, v52
	v_sub_f32_e32 v71, v71, v52
	v_sub_f32_e32 v70, v70, v52
	v_sub_f32_e32 v69, v69, v52
	v_sub_f32_e32 v68, v68, v52
	v_sub_f32_e32 v51, v51, v52
	v_sub_f32_e32 v50, v50, v52
	v_sub_f32_e32 v49, v49, v52
	v_sub_f32_e32 v48, v48, v52
	v_sub_f32_e32 v47, v47, v52
	v_sub_f32_e32 v46, v46, v52
	v_sub_f32_e32 v45, v45, v52
	v_sub_f32_e32 v44, v44, v52
	v_sub_f32_e32 v43, v43, v52
	v_sub_f32_e32 v42, v42, v52
	v_sub_f32_e32 v41, v41, v52
	v_sub_f32_e32 v40, v40, v52
	v_sub_f32_e32 v39, v39, v52
	v_sub_f32_e32 v38, v38, v52
	v_sub_f32_e32 v37, v37, v52
	v_sub_f32_e32 v36, v36, v52

.LBB0_1675:
	s_xor_b32 s2, s26, 2
	s_mulk_i32 s2, 0x3000
	v_add_u32_e32 v56, s2, v151
	ds_read_b128 v[52:55], v56
	ds_read_b128 v[156:159], v56 offset:512
	ds_read_b128 v[160:163], v56 offset:2048
	ds_read_b128 v[164:167], v56 offset:2560
	ds_read_b128 v[168:171], v56 offset:4096
	ds_read_b128 v[172:175], v56 offset:4608
	ds_read_b128 v[176:179], v56 offset:6144
	ds_read_b128 v[180:183], v56 offset:6656
	ds_read_b128 v[184:187], v56 offset:8192
	ds_read_b128 v[190:193], v56 offset:8704
	ds_read_b128 v[212:215], v56 offset:10240
	ds_read_b128 v[216:219], v56 offset:10752
	s_waitcnt lgkmcnt(11)
	v_mfma_f32_32x32x16_bf16 v[84:99], v[52:55], v[116:119], v[36:51]
	v_exp_f32_e32 v100, v100
	v_exp_f32_e32 v101, v101
	v_exp_f32_e32 v102, v102
	v_exp_f32_e32 v103, v103
	s_waitcnt lgkmcnt(10)
	v_mfma_f32_32x32x16_bf16 v[52:67], v[156:159], v[116:119], v[36:51]
	v_add_f32_e64 v156, v100, 0
	v_add_f32_e64 v157, v101, 0
	v_add_f32_e64 v156, v102, v156
	v_add_f32_e64 v157, v103, v157
	s_waitcnt lgkmcnt(9)
	v_mfma_f32_32x32x16_bf16 v[84:99], v[160:163], v[120:123], v[84:99]
	v_exp_f32_e32 v104, v104
	v_exp_f32_e32 v105, v105
	v_exp_f32_e32 v106, v106
	v_exp_f32_e32 v107, v107
	v_add_f32_e32 v156, v104, v156
	v_add_f32_e32 v157, v105, v157
	v_add_f32_e32 v156, v106, v156
	v_add_f32_e32 v157, v107, v157
	s_waitcnt lgkmcnt(8)
	v_mfma_f32_32x32x16_bf16 v[52:67], v[164:167], v[120:123], v[52:67]
	s_waitcnt lgkmcnt(7)
	v_mfma_f32_32x32x16_bf16 v[84:99], v[168:171], v[124:127], v[84:99]
	v_exp_f32_e32 v108, v108
	v_exp_f32_e32 v109, v109
	v_exp_f32_e32 v110, v110
	v_exp_f32_e32 v111, v111
	v_add_f32_e32 v156, v108, v156
	v_add_f32_e32 v157, v109, v157
	v_add_f32_e32 v156, v110, v156
	v_add_f32_e32 v157, v111, v157
	s_waitcnt lgkmcnt(6)
	v_mfma_f32_32x32x16_bf16 v[52:67], v[172:175], v[124:127], v[52:67]
	s_waitcnt lgkmcnt(5)
	v_mfma_f32_32x32x16_bf16 v[84:99], v[176:179], v[128:131], v[84:99]
	v_exp_f32_e32 v112, v112
	v_exp_f32_e32 v113, v113
	v_exp_f32_e32 v114, v114
	v_exp_f32_e32 v115, v115
	v_add_f32_e32 v156, v112, v156
	v_add_f32_e32 v157, v113, v157
	v_add_f32_e32 v156, v114, v156
	v_add_f32_e32 v157, v115, v157
	s_waitcnt lgkmcnt(4)
	v_mfma_f32_32x32x16_bf16 v[52:67], v[180:183], v[128:131], v[52:67]
	v_exp_f32_e32 v158, v68
	v_exp_f32_e32 v159, v69
	s_waitcnt lgkmcnt(3)
	v_mfma_f32_32x32x16_bf16 v[84:99], v[184:187], v[132:135], v[84:99]
	v_add_f32_e64 v68, v158, v156
	v_add_f32_e64 v69, v159, v157
	v_exp_f32_e32 v156, v70
	v_exp_f32_e32 v157, v71
	v_add_f32_e32 v68, v156, v68
	v_add_f32_e32 v69, v157, v69
	s_waitcnt lgkmcnt(2)
	v_mfma_f32_32x32x16_bf16 v[52:67], v[190:193], v[132:135], v[52:67]
	s_waitcnt lgkmcnt(1)
	v_mfma_f32_32x32x16_bf16 v[84:99], v[212:215], v[136:139], v[84:99]
	v_exp_f32_e32 v160, v72
	v_exp_f32_e32 v161, v73
	v_exp_f32_e32 v162, v74
	v_exp_f32_e32 v163, v75
	v_add_f32_e32 v68, v160, v68
	v_add_f32_e32 v69, v161, v69
	v_add_f32_e32 v176, v162, v68
	v_add_f32_e32 v177, v163, v69
	s_waitcnt lgkmcnt(0)
	v_mfma_f32_32x32x16_bf16 v[52:67], v[216:219], v[136:139], v[52:67]
	v_cvt_pk_bf16_f32 v70, v104, v105
	v_lshl_add_u32 v155, s25, 13, v2
	ds_read_b64_tr_b16 v[104:105],v155 offset:0
	v_cvt_pk_bf16_f32 v71, v106, v107
	ds_read_b64_tr_b16 v[106:107],v155 offset:512
	v_cvt_pk_bf16_f32 v69, v102, v103
	v_cvt_pk_bf16_f32 v102, v160, v161
	ds_read_b64_tr_b16 v[160:161],v155 offset:4096
	v_cvt_pk_bf16_f32 v103, v162, v163
	ds_read_b64_tr_b16 v[162:163],v155 offset:4608
	v_cvt_pk_bf16_f32 v72, v108, v109
	ds_read_b64_tr_b16 v[108:109],v155 offset:1024
	v_cvt_pk_bf16_f32 v73, v110, v111
	ds_read_b64_tr_b16 v[110:111],v155 offset:1536
	ds_read_b64_tr_b16 v[164:165],v155 offset:5120
	ds_read_b64_tr_b16 v[166:167],v155 offset:5632
	v_cvt_pk_bf16_f32 v74, v112, v113
	ds_read_b64_tr_b16 v[112:113],v155 offset:2048
	v_cvt_pk_bf16_f32 v75, v114, v115
	ds_read_b64_tr_b16 v[114:115],v155 offset:2560
	ds_read_b64_tr_b16 v[168:169],v155 offset:6144
	ds_read_b64_tr_b16 v[170:171],v155 offset:6656
	v_cvt_pk_bf16_f32 v68, v100, v101
	v_cvt_pk_bf16_f32 v101, v156, v157
	ds_read_b64_tr_b16 v[156:157],v155 offset:3072
	v_cvt_pk_bf16_f32 v100, v158, v159
	ds_read_b64_tr_b16 v[158:159],v155 offset:3584
	ds_read_b64_tr_b16 v[172:173],v155 offset:7168
	ds_read_b64_tr_b16 v[174:175],v155 offset:7680
	s_waitcnt lgkmcnt(14)
	v_mfma_f32_32x32x16_bf16 v[4:19], v[68:71], v[104:107], v[4:19]
	s_waitcnt lgkmcnt(12)
	v_mfma_f32_32x32x16_bf16 v[20:35], v[68:71], v[160:163], v[20:35]
	v_exp_f32_e32 v68, v76
	v_exp_f32_e32 v69, v77
	v_exp_f32_e32 v76, v78
	v_exp_f32_e32 v77, v79
	v_add_f32_e32 v70, v68, v176
	v_add_f32_e32 v71, v69, v177
	v_add_f32_e32 v70, v76, v70
	v_add_f32_e32 v71, v77, v71
	s_waitcnt lgkmcnt(10)
	v_mfma_f32_32x32x16_bf16 v[4:19], v[72:75], v[108:111], v[4:19]
	v_cvt_pk_bf16_f32 v68, v68, v69
	v_cvt_pk_bf16_f32 v69, v76, v77
	s_waitcnt lgkmcnt(8)
	v_mfma_f32_32x32x16_bf16 v[20:35], v[72:75], v[164:167], v[20:35]
	v_exp_f32_e32 v72, v80
	v_exp_f32_e32 v73, v81
	v_exp_f32_e32 v74, v82
	v_exp_f32_e32 v75, v83
	v_add_f32_e32 v70, v72, v70
	v_add_f32_e32 v71, v73, v71
	v_add_f32_e32 v78, v74, v70
	v_add_f32_e32 v79, v75, v71
	v_cvt_pk_bf16_f32 v70, v72, v73
	v_add_f32_e32 v72, v78, v79
	v_add_f32_e32 v154, v154, v72
	v_cvt_pk_bf16_f32 v71, v74, v75
	s_waitcnt lgkmcnt(6)
	v_mfma_f32_32x32x16_bf16 v[4:19], v[100:103], v[112:115], v[4:19]
	v_max3_f32 v72, v84, v52, v85
	v_max3_f32 v72, v72, v53, v86
	v_max3_f32 v72, v72, v54, v87
	v_max3_f32 v72, v72, v55, v88
	s_waitcnt lgkmcnt(4)
	v_mfma_f32_32x32x16_bf16 v[20:35], v[100:103], v[168:171], v[20:35]
	v_max3_f32 v72, v72, v56, v89
	v_max3_f32 v72, v72, v57, v90
	v_max3_f32 v72, v72, v58, v91
	v_max3_f32 v72, v72, v59, v91
	s_waitcnt lgkmcnt(2)
	v_mfma_f32_32x32x16_bf16 v[4:19], v[68:71], v[156:159], v[4:19]
	s_waitcnt lgkmcnt(0)
	v_mfma_f32_32x32x16_bf16 v[20:35], v[68:71], v[172:175], v[20:35]
	v_max3_f32 v68, v72, v92, v60
	v_max3_f32 v68, v68, v93, v61
	v_max3_f32 v68, v68, v94, v62
	v_max3_f32 v68, v68, v95, v63
	v_max3_f32 v68, v68, v96, v64
	v_max3_f32 v68, v68, v97, v65
	v_max3_f32 v68, v68, v98, v66
	v_max3_f32 v68, v68, v99, v67
	v_mov_b32_e32 v69, v68
	s_nop 1
	v_permlane32_swap_b32_e32 v68, v69
	s_and_b64 vcc, exec, s[38:39]
	s_cbranch_vccnz .LBB0_1662
	v_max_f32_e32 v68, v68, v68
	v_max_f32_e32 v69, v69, v69
	v_max_f32_e32 v68, v68, v69
	v_cmp_lt_f32_e32 vcc, s13, v68
	s_cbranch_vccz .LBB0_1662
	v_max_f32_e32 v68, v68, v68
	v_max_f32_e32 v68, 0, v68
	v_exp_f32_e64 v69, -v68
	s_and_saveexec_b64 s[6:7], s[36:37]
	s_cbranch_execz .LBB0_1661
	ds_write_b32 v153, v69
	s_branch .LBB0_1661
